# v22_storediag
# speedup vs baseline: 1.0160x; 1.0085x over previous
.LBB1_320:
	v_or_b32_e32 v13, 0xffffff00, v0
	v_lshrrev_b32_e32 v38, 6, v0
	v_lshlrev_b32_e32 v0, 2, v108
	s_movk_i32 s52, 0x110
	v_mul_u32_u24_e32 v1, 0x10c, v108
	v_mad_u32_u24 v39, v38, s52, v0
	v_lshlrev_b32_e32 v2, 2, v38
	s_mul_i32 s52, s64, 0x8040
	v_add3_u32 v40, v1, v2, v0
	v_lshl_add_u32 v0, v38, 9, s52
	v_or_b32_e32 v44, v0, v108
	s_mov_b64 s[52:53], 0
	s_movk_i32 s65, 0xeff
	v_mov_b32_e32 v2, v38
	v_mov_b32_e32 v0, v44
	v_mov_b32_e32 v3, v40
	v_mov_b32_e32 v4, v39
	v_mov_b32_e32 v5, v13
	s_waitcnt lgkmcnt(0)
	s_barrier
	v_lshlrev_b32_e32 v0, 2, v0
	v_add_u32_e32 v1, 0x1dc00, v4
	ds_read_b32 v54, v1
	ds_read_b32 v55, v4
	ds_read_b32 v56, v3
	ds_read_b32 v57, v1 offset:1088
	ds_read_b32 v58, v4 offset:1088
	ds_read_b32 v59, v3 offset:16
	ds_read_b32 v60, v1 offset:2176
	ds_read_b32 v61, v4 offset:2176
	ds_read_b32 v62, v3 offset:32
	ds_read_b32 v63, v1 offset:3264
	ds_read_b32 v64, v4 offset:3264
	ds_read_b32 v65, v3 offset:48
	v_cmp_ge_u32_e32 vcc, v2, v108
	v_add_u32_e32 v2, 4, v2
	s_waitcnt lgkmcnt(9)
	v_cndmask_b32_e32 v54, 0, v54, vcc
	global_store_dword v0, v54, s[66:67]
	global_store_dword v0, v55, s[60:61]
	global_store_dword v0, v56, s[62:63]
	v_add_u32_e32 v0, 0x2000, v0
	v_cmp_ge_u32_e32 vcc, v2, v108
	v_add_u32_e32 v2, 4, v2
	s_waitcnt lgkmcnt(6)
	v_cndmask_b32_e32 v57, 0, v57, vcc
	global_store_dword v0, v57, s[66:67]
	global_store_dword v0, v58, s[60:61]
	global_store_dword v0, v59, s[62:63]
	v_add_u32_e32 v0, 0x2000, v0
	v_cmp_ge_u32_e32 vcc, v2, v108
	v_add_u32_e32 v2, 4, v2
	s_waitcnt lgkmcnt(3)
	v_cndmask_b32_e32 v60, 0, v60, vcc
	global_store_dword v0, v60, s[66:67]
	global_store_dword v0, v61, s[60:61]
	global_store_dword v0, v62, s[62:63]
	v_add_u32_e32 v0, 0x2000, v0
	v_cmp_ge_u32_e32 vcc, v2, v108
	v_add_u32_e32 v2, 4, v2
	s_waitcnt lgkmcnt(0)
	v_cndmask_b32_e32 v63, 0, v63, vcc
	global_store_dword v0, v63, s[66:67]
	global_store_dword v0, v64, s[60:61]
	global_store_dword v0, v65, s[62:63]
	v_add_u32_e32 v0, 0x2000, v0
	ds_read_b32 v54, v1 offset:4352
	ds_read_b32 v55, v4 offset:4352
	ds_read_b32 v56, v3 offset:64
	ds_read_b32 v57, v1 offset:5440
	ds_read_b32 v58, v4 offset:5440
	ds_read_b32 v59, v3 offset:80
	ds_read_b32 v60, v1 offset:6528
	ds_read_b32 v61, v4 offset:6528
	ds_read_b32 v62, v3 offset:96
	ds_read_b32 v63, v1 offset:7616
	ds_read_b32 v64, v4 offset:7616
	ds_read_b32 v65, v3 offset:112
	v_cmp_ge_u32_e32 vcc, v2, v108
	v_add_u32_e32 v2, 4, v2
	s_waitcnt lgkmcnt(9)
	v_cndmask_b32_e32 v54, 0, v54, vcc
	global_store_dword v0, v54, s[66:67]
	global_store_dword v0, v55, s[60:61]
	global_store_dword v0, v56, s[62:63]
	v_add_u32_e32 v0, 0x2000, v0
	v_cmp_ge_u32_e32 vcc, v2, v108
	v_add_u32_e32 v2, 4, v2
	s_waitcnt lgkmcnt(6)
	v_cndmask_b32_e32 v57, 0, v57, vcc
	global_store_dword v0, v57, s[66:67]
	global_store_dword v0, v58, s[60:61]
	global_store_dword v0, v59, s[62:63]
	v_add_u32_e32 v0, 0x2000, v0
	v_cmp_ge_u32_e32 vcc, v2, v108
	v_add_u32_e32 v2, 4, v2
	s_waitcnt lgkmcnt(3)
	v_cndmask_b32_e32 v60, 0, v60, vcc
	global_store_dword v0, v60, s[66:67]
	global_store_dword v0, v61, s[60:61]
	global_store_dword v0, v62, s[62:63]
	v_add_u32_e32 v0, 0x2000, v0
	v_cmp_ge_u32_e32 vcc, v2, v108
	v_add_u32_e32 v2, 4, v2
	s_waitcnt lgkmcnt(0)
	v_cndmask_b32_e32 v63, 0, v63, vcc
	global_store_dword v0, v63, s[66:67]
	global_store_dword v0, v64, s[60:61]
	global_store_dword v0, v65, s[62:63]
	v_add_u32_e32 v0, 0x2000, v0
	ds_read_b32 v54, v1 offset:8704
	ds_read_b32 v55, v4 offset:8704
	ds_read_b32 v56, v3 offset:128
	ds_read_b32 v57, v1 offset:9792
	ds_read_b32 v58, v4 offset:9792
	ds_read_b32 v59, v3 offset:144
	ds_read_b32 v60, v1 offset:10880
	ds_read_b32 v61, v4 offset:10880
	ds_read_b32 v62, v3 offset:160
	ds_read_b32 v63, v1 offset:11968
	ds_read_b32 v64, v4 offset:11968
	ds_read_b32 v65, v3 offset:176
	v_cmp_ge_u32_e32 vcc, v2, v108
	v_add_u32_e32 v2, 4, v2
	s_waitcnt lgkmcnt(9)
	v_cndmask_b32_e32 v54, 0, v54, vcc
	global_store_dword v0, v54, s[66:67]
	global_store_dword v0, v55, s[60:61]
	global_store_dword v0, v56, s[62:63]
	v_add_u32_e32 v0, 0x2000, v0
	v_cmp_ge_u32_e32 vcc, v2, v108
	v_add_u32_e32 v2, 4, v2
	s_waitcnt lgkmcnt(6)
	v_cndmask_b32_e32 v57, 0, v57, vcc
	global_store_dword v0, v57, s[66:67]
	global_store_dword v0, v58, s[60:61]
	global_store_dword v0, v59, s[62:63]
	v_add_u32_e32 v0, 0x2000, v0
	v_cmp_ge_u32_e32 vcc, v2, v108
	v_add_u32_e32 v2, 4, v2
	s_waitcnt lgkmcnt(3)
	v_cndmask_b32_e32 v60, 0, v60, vcc
	global_store_dword v0, v60, s[66:67]
	global_store_dword v0, v61, s[60:61]
	global_store_dword v0, v62, s[62:63]
	v_add_u32_e32 v0, 0x2000, v0
	v_cmp_ge_u32_e32 vcc, v2, v108
	v_add_u32_e32 v2, 4, v2
	s_waitcnt lgkmcnt(0)
	v_cndmask_b32_e32 v63, 0, v63, vcc
	global_store_dword v0, v63, s[66:67]
	global_store_dword v0, v64, s[60:61]
	global_store_dword v0, v65, s[62:63]
	v_add_u32_e32 v0, 0x2000, v0
	ds_read_b32 v54, v1 offset:13056
	ds_read_b32 v55, v4 offset:13056
	ds_read_b32 v56, v3 offset:192
	ds_read_b32 v57, v1 offset:14144
	ds_read_b32 v58, v4 offset:14144
	ds_read_b32 v59, v3 offset:208
	ds_read_b32 v60, v1 offset:15232
	ds_read_b32 v61, v4 offset:15232
	ds_read_b32 v62, v3 offset:224
	ds_read_b32 v63, v1 offset:16320
	ds_read_b32 v64, v4 offset:16320
	ds_read_b32 v65, v3 offset:240
	v_cmp_ge_u32_e32 vcc, v2, v108
	v_add_u32_e32 v2, 4, v2
	s_waitcnt lgkmcnt(9)
	v_cndmask_b32_e32 v54, 0, v54, vcc
	global_store_dword v0, v54, s[66:67]
	global_store_dword v0, v55, s[60:61]
	global_store_dword v0, v56, s[62:63]
	v_add_u32_e32 v0, 0x2000, v0
	v_cmp_ge_u32_e32 vcc, v2, v108
	v_add_u32_e32 v2, 4, v2
	s_waitcnt lgkmcnt(6)
	v_cndmask_b32_e32 v57, 0, v57, vcc
	global_store_dword v0, v57, s[66:67]
	global_store_dword v0, v58, s[60:61]
	global_store_dword v0, v59, s[62:63]
	v_add_u32_e32 v0, 0x2000, v0
	v_cmp_ge_u32_e32 vcc, v2, v108
	v_add_u32_e32 v2, 4, v2
	s_waitcnt lgkmcnt(3)
	v_cndmask_b32_e32 v60, 0, v60, vcc
	global_store_dword v0, v60, s[66:67]
	global_store_dword v0, v61, s[60:61]
	global_store_dword v0, v62, s[62:63]
	v_add_u32_e32 v0, 0x2000, v0
	v_cmp_ge_u32_e32 vcc, v2, v108
	v_add_u32_e32 v2, 4, v2
	s_waitcnt lgkmcnt(0)
	v_cndmask_b32_e32 v63, 0, v63, vcc
	global_store_dword v0, v63, s[66:67]
	global_store_dword v0, v64, s[60:61]
	global_store_dword v0, v65, s[62:63]
	v_add_u32_e32 v0, 0x2000, v0

.LBB1_361:
	v_add_u32_e32 v0, 0x8040, v44
	s_mov_b64 s[0:1], 0
	s_movk_i32 s4, 0xeff
	s_waitcnt lgkmcnt(0)
	s_barrier
	v_lshlrev_b32_e32 v0, 2, v0
	v_add_u32_e32 v1, 0x19800, v39
	ds_read_b32 v54, v1
	ds_read_b32 v55, v39
	ds_read_b32 v56, v40
	ds_read_b32 v57, v1 offset:1088
	ds_read_b32 v58, v39 offset:1088
	ds_read_b32 v59, v40 offset:16
	ds_read_b32 v60, v1 offset:2176
	ds_read_b32 v61, v39 offset:2176
	ds_read_b32 v62, v40 offset:32
	ds_read_b32 v63, v1 offset:3264
	ds_read_b32 v64, v39 offset:3264
	ds_read_b32 v65, v40 offset:48
	v_cmp_ge_u32_e32 vcc, v38, v108
	v_add_u32_e32 v38, 4, v38
	s_waitcnt lgkmcnt(9)
	v_cndmask_b32_e32 v54, 0, v54, vcc
	global_store_dword v0, v54, s[66:67]
	global_store_dword v0, v55, s[60:61]
	global_store_dword v0, v56, s[62:63]
	v_add_u32_e32 v0, 0x2000, v0
	v_cmp_ge_u32_e32 vcc, v38, v108
	v_add_u32_e32 v38, 4, v38
	s_waitcnt lgkmcnt(6)
	v_cndmask_b32_e32 v57, 0, v57, vcc
	global_store_dword v0, v57, s[66:67]
	global_store_dword v0, v58, s[60:61]
	global_store_dword v0, v59, s[62:63]
	v_add_u32_e32 v0, 0x2000, v0
	v_cmp_ge_u32_e32 vcc, v38, v108
	v_add_u32_e32 v38, 4, v38
	s_waitcnt lgkmcnt(3)
	v_cndmask_b32_e32 v60, 0, v60, vcc
	global_store_dword v0, v60, s[66:67]
	global_store_dword v0, v61, s[60:61]
	global_store_dword v0, v62, s[62:63]
	v_add_u32_e32 v0, 0x2000, v0
	v_cmp_ge_u32_e32 vcc, v38, v108
	v_add_u32_e32 v38, 4, v38
	s_waitcnt lgkmcnt(0)
	v_cndmask_b32_e32 v63, 0, v63, vcc
	global_store_dword v0, v63, s[66:67]
	global_store_dword v0, v64, s[60:61]
	global_store_dword v0, v65, s[62:63]
	v_add_u32_e32 v0, 0x2000, v0
	ds_read_b32 v54, v1 offset:4352
	ds_read_b32 v55, v39 offset:4352
	ds_read_b32 v56, v40 offset:64
	ds_read_b32 v57, v1 offset:5440
	ds_read_b32 v58, v39 offset:5440
	ds_read_b32 v59, v40 offset:80
	ds_read_b32 v60, v1 offset:6528
	ds_read_b32 v61, v39 offset:6528
	ds_read_b32 v62, v40 offset:96
	ds_read_b32 v63, v1 offset:7616
	ds_read_b32 v64, v39 offset:7616
	ds_read_b32 v65, v40 offset:112
	v_cmp_ge_u32_e32 vcc, v38, v108
	v_add_u32_e32 v38, 4, v38
	s_waitcnt lgkmcnt(9)
	v_cndmask_b32_e32 v54, 0, v54, vcc
	global_store_dword v0, v54, s[66:67]
	global_store_dword v0, v55, s[60:61]
	global_store_dword v0, v56, s[62:63]
	v_add_u32_e32 v0, 0x2000, v0
	v_cmp_ge_u32_e32 vcc, v38, v108
	v_add_u32_e32 v38, 4, v38
	s_waitcnt lgkmcnt(6)
	v_cndmask_b32_e32 v57, 0, v57, vcc
	global_store_dword v0, v57, s[66:67]
	global_store_dword v0, v58, s[60:61]
	global_store_dword v0, v59, s[62:63]
	v_add_u32_e32 v0, 0x2000, v0
	v_cmp_ge_u32_e32 vcc, v38, v108
	v_add_u32_e32 v38, 4, v38
	s_waitcnt lgkmcnt(3)
	v_cndmask_b32_e32 v60, 0, v60, vcc
	global_store_dword v0, v60, s[66:67]
	global_store_dword v0, v61, s[60:61]
	global_store_dword v0, v62, s[62:63]
	v_add_u32_e32 v0, 0x2000, v0
	v_cmp_ge_u32_e32 vcc, v38, v108
	v_add_u32_e32 v38, 4, v38
	s_waitcnt lgkmcnt(0)
	v_cndmask_b32_e32 v63, 0, v63, vcc
	global_store_dword v0, v63, s[66:67]
	global_store_dword v0, v64, s[60:61]
	global_store_dword v0, v65, s[62:63]
	v_add_u32_e32 v0, 0x2000, v0
	ds_read_b32 v54, v1 offset:8704
	ds_read_b32 v55, v39 offset:8704
	ds_read_b32 v56, v40 offset:128
	ds_read_b32 v57, v1 offset:9792
	ds_read_b32 v58, v39 offset:9792
	ds_read_b32 v59, v40 offset:144
	ds_read_b32 v60, v1 offset:10880
	ds_read_b32 v61, v39 offset:10880
	ds_read_b32 v62, v40 offset:160
	ds_read_b32 v63, v1 offset:11968
	ds_read_b32 v64, v39 offset:11968
	ds_read_b32 v65, v40 offset:176
	v_cmp_ge_u32_e32 vcc, v38, v108
	v_add_u32_e32 v38, 4, v38
	s_waitcnt lgkmcnt(9)
	v_cndmask_b32_e32 v54, 0, v54, vcc
	global_store_dword v0, v54, s[66:67]
	global_store_dword v0, v55, s[60:61]
	global_store_dword v0, v56, s[62:63]
	v_add_u32_e32 v0, 0x2000, v0
	v_cmp_ge_u32_e32 vcc, v38, v108
	v_add_u32_e32 v38, 4, v38
	s_waitcnt lgkmcnt(6)
	v_cndmask_b32_e32 v57, 0, v57, vcc
	global_store_dword v0, v57, s[66:67]
	global_store_dword v0, v58, s[60:61]
	global_store_dword v0, v59, s[62:63]
	v_add_u32_e32 v0, 0x2000, v0
	v_cmp_ge_u32_e32 vcc, v38, v108
	v_add_u32_e32 v38, 4, v38
	s_waitcnt lgkmcnt(3)
	v_cndmask_b32_e32 v60, 0, v60, vcc
	global_store_dword v0, v60, s[66:67]
	global_store_dword v0, v61, s[60:61]
	global_store_dword v0, v62, s[62:63]
	v_add_u32_e32 v0, 0x2000, v0
	v_cmp_ge_u32_e32 vcc, v38, v108
	v_add_u32_e32 v38, 4, v38
	s_waitcnt lgkmcnt(0)
	v_cndmask_b32_e32 v63, 0, v63, vcc
	global_store_dword v0, v63, s[66:67]
	global_store_dword v0, v64, s[60:61]
	global_store_dword v0, v65, s[62:63]
	v_add_u32_e32 v0, 0x2000, v0
	ds_read_b32 v54, v1 offset:13056
	ds_read_b32 v55, v39 offset:13056
	ds_read_b32 v56, v40 offset:192
	ds_read_b32 v57, v1 offset:14144
	ds_read_b32 v58, v39 offset:14144
	ds_read_b32 v59, v40 offset:208
	ds_read_b32 v60, v1 offset:15232
	ds_read_b32 v61, v39 offset:15232
	ds_read_b32 v62, v40 offset:224
	ds_read_b32 v63, v1 offset:16320
	ds_read_b32 v64, v39 offset:16320
	ds_read_b32 v65, v40 offset:240
	v_cmp_ge_u32_e32 vcc, v38, v108
	v_add_u32_e32 v38, 4, v38
	s_waitcnt lgkmcnt(9)
	v_cndmask_b32_e32 v54, 0, v54, vcc
	global_store_dword v0, v54, s[66:67]
	global_store_dword v0, v55, s[60:61]
	global_store_dword v0, v56, s[62:63]
	v_add_u32_e32 v0, 0x2000, v0
	v_cmp_ge_u32_e32 vcc, v38, v108
	v_add_u32_e32 v38, 4, v38
	s_waitcnt lgkmcnt(6)
	v_cndmask_b32_e32 v57, 0, v57, vcc
	global_store_dword v0, v57, s[66:67]
	global_store_dword v0, v58, s[60:61]
	global_store_dword v0, v59, s[62:63]
	v_add_u32_e32 v0, 0x2000, v0
	v_cmp_ge_u32_e32 vcc, v38, v108
	v_add_u32_e32 v38, 4, v38
	s_waitcnt lgkmcnt(3)
	v_cndmask_b32_e32 v60, 0, v60, vcc
	global_store_dword v0, v60, s[66:67]
	global_store_dword v0, v61, s[60:61]
	global_store_dword v0, v62, s[62:63]
	v_add_u32_e32 v0, 0x2000, v0
	v_cmp_ge_u32_e32 vcc, v38, v108
	v_add_u32_e32 v38, 4, v38
	s_waitcnt lgkmcnt(0)
	v_cndmask_b32_e32 v63, 0, v63, vcc
	global_store_dword v0, v63, s[66:67]
	global_store_dword v0, v64, s[60:61]
	global_store_dword v0, v65, s[62:63]
	v_add_u32_e32 v0, 0x2000, v0
